# wt4+awr+akf + attention instruction trims (32-bit saddr prefetch addressing, packed output scaling, no self-max)
# speedup vs baseline: 1.0116x; 1.0116x over previous
.LBB0_412:
	s_and_b32 s49, s38, 1
	s_mul_i32 s101, s49, 0x12000
	v_add3_u32 v56, s101, v182, v215
	v_add3_u32 v64, s101, v183, v215
	ds_read_b128 v[52:55], v56
	ds_read_b128 v[56:59], v56 offset:64
	ds_read_b128 v[60:63], v64
	ds_read_b128 v[66:69], v64 offset:64
	v_add3_u32 v64, s101, v184, v215
	ds_read_b128 v[70:73], v64
	ds_read_b128 v[74:77], v64 offset:64
	v_add3_u32 v64, s101, v185, v215
	ds_read_b128 v[90:93], v64
	ds_read_b128 v[94:97], v64 offset:64
	v_add3_u32 v64, s101, v186, v215
	ds_read_b128 v[98:101], v64
	ds_read_b128 v[102:105], v64 offset:64
	v_add3_u32 v64, s101, v187, v215
	ds_read_b128 v[106:109], v64
	ds_read_b128 v[110:113], v64 offset:64
	v_add3_u32 v64, s101, v188, v215
	ds_read_b128 v[114:117], v64
	ds_read_b128 v[118:121], v64 offset:64
	v_add3_u32 v64, s101, v189, v215
	ds_read_b128 v[122:125], v64
	ds_read_b128 v[126:129], v64 offset:64
	v_add3_u32 v64, s101, v190, v215
	ds_read_b128 v[130:133], v64
	ds_read_b128 v[134:137], v64 offset:64
	s_mul_hi_i32 s23, s39, 0x2aaaaaab
	s_lshr_b32 s24, s23, 31
	s_ashr_i32 s23, s23, 5
	s_add_i32 s34, s23, s24
	s_mul_i32 s23, s34, 0xffffff40
	s_add_i32 s23, s39, s23
	s_mov_b32 s31, s25
	s_and_b32 s49, s38, 1
	s_xor_b32 s100, s49, 1
	s_mul_i32 s100, s100, 0x12000
	s_ashr_i32 s24, s23, 6
	s_and_b32 s25, s39, 63
	s_ashr_i32 s36, s34, 4
	s_cmp_eq_u32 s24, 1
	s_cselect_b64 s[26:27], -1, 0
	s_and_b64 s[28:29], s[26:27], exec
	s_cselect_b32 s35, 3, 15
	s_cselect_b32 s37, 2, 4
	s_cmp_lt_u32 s23, 64
	s_cselect_b64 s[28:29], -1, 0
	s_and_b64 s[56:57], s[28:29], exec
	s_cselect_b32 s62, 0, s37
	s_waitcnt vmcnt(2)
	v_mov_b64_e32 v[88:89], v[10:11]
	s_cselect_b32 s23, 0, s35
	s_lshr_b32 s25, s25, s62
	s_waitcnt vmcnt(1)
	v_mov_b64_e32 v[50:51], v[14:15]
	v_mov_b64_e32 v[86:87], v[8:9]
	v_sub_u32_e64 v8, s25, 1 clamp
	v_mov_b64_e32 v[48:49], v[12:13]
	s_ashr_i32 s35, s34, 31
	v_lshlrev_b32_e32 v12, 7, v8
	s_and_b32 s23, s23, s70
	s_lshl_b64 s[56:57], s[34:35], 13
	s_or_b32 s56, s56, s23
	v_mov_b32_e32 v204, s56
	v_or_b32_e32 v8, v12, v172
	v_lshl_add_u32 v8, v8, s62, v204
	v_lshl_or_b32 v8, v8, 7, v191
	global_load_dwordx4 v[16:19], v8, s[76:77]
	global_load_dwordx4 v[20:23], v8, s[78:79]
	v_or_b32_e32 v8, v12, v174
	v_lshl_add_u32 v8, v8, s62, v204
	v_lshl_or_b32 v8, v8, 7, v191
	s_lshl_b32 s63, s25, 7
	global_load_dwordx4 v[24:27], v8, s[76:77]
	global_load_dwordx4 v[28:31], v8, s[78:79]
	v_or_b32_e32 v8, s63, v172
	v_lshl_add_u32 v8, v8, s62, v204
	v_lshl_or_b32 v8, v8, 7, v191
	global_load_dwordx4 v[32:35], v8, s[76:77]
	global_load_dwordx4 v[36:39], v8, s[78:79]
	v_or_b32_e32 v8, s63, v175
	v_lshl_add_u32 v8, v8, s62, v204
	v_lshl_or_b32 v8, v8, 7, v191
	global_load_dwordx4 v[40:43], v8, s[76:77]
	global_load_dwordx4 v[44:47], v8, s[78:79]
	s_ashr_i32 s37, s36, 31
	v_add_u32_e32 v8, s63, v181
	s_lshl_b64 s[36:37], s[36:37], 13
	v_ashrrev_i32_e32 v9, 31, v8
	s_or_b32 s36, s36, s23
	v_lshlrev_b64 v[8:9], s62, v[8:9]
	v_lshl_add_u64 v[164:165], s[36:37], 0, v[8:9]
	v_lshlrev_b64 v[162:163], 6, v[164:165]
	s_lshl_b64 s[36:37], s[34:35], 20
	s_add_u32 s36, s64, s36
	v_lshlrev_b32_e32 v8, 1, v162
	s_addc_u32 s37, s65, s37
	v_and_b32_e32 v64, 0xfff80, v8
	v_lshl_add_u64 v[8:9], s[36:37], 0, v[64:65]
	v_mov_b32_e32 v169, v65
	v_lshl_add_u64 v[12:13], v[8:9], 0, v[168:169]
	global_load_dwordx4 v[8:11], v[12:13], off
	s_nop 0
	global_load_dwordx4 v[12:15], v[12:13], off offset:64
	s_waitcnt lgkmcnt(14)
	v_mfma_f32_16x16x32_bf16 v[52:55], v[52:55], v[86:89], v[4:7]
	s_cmp_lg_u32 s31, 0
	v_mfma_f32_16x16x32_bf16 v[82:85], v[56:59], v[48:51], v[52:55]
	v_mfma_f32_16x16x32_bf16 v[52:55], v[60:63], v[86:89], 0
	v_mfma_f32_16x16x32_bf16 v[78:81], v[66:69], v[48:51], v[52:55]
	s_waitcnt lgkmcnt(13)
	v_mfma_f32_16x16x32_bf16 v[52:55], v[70:73], v[86:89], 0
	s_waitcnt lgkmcnt(12)
	v_mfma_f32_16x16x32_bf16 v[74:77], v[74:77], v[48:51], v[52:55]
	s_waitcnt lgkmcnt(11)
	v_mfma_f32_16x16x32_bf16 v[52:55], v[90:93], v[86:89], 0
	s_waitcnt lgkmcnt(10)
	v_mfma_f32_16x16x32_bf16 v[70:73], v[94:97], v[48:51], v[52:55]
	s_waitcnt lgkmcnt(9)
	v_mfma_f32_16x16x32_bf16 v[52:55], v[98:101], v[86:89], 0
	s_waitcnt lgkmcnt(8)
	v_mfma_f32_16x16x32_bf16 v[66:69], v[102:105], v[48:51], v[52:55]
	s_waitcnt lgkmcnt(7)
	v_mfma_f32_16x16x32_bf16 v[52:55], v[106:109], v[86:89], 0
	s_waitcnt lgkmcnt(6)
	v_mfma_f32_16x16x32_bf16 v[60:63], v[110:113], v[48:51], v[52:55]
	s_waitcnt lgkmcnt(5)
	v_mfma_f32_16x16x32_bf16 v[52:55], v[114:117], v[86:89], 0
	s_waitcnt lgkmcnt(4)
	v_mfma_f32_16x16x32_bf16 v[56:59], v[118:121], v[48:51], v[52:55]
	s_waitcnt lgkmcnt(3)
	v_mfma_f32_16x16x32_bf16 v[52:55], v[122:125], v[86:89], 0
	s_waitcnt lgkmcnt(1)
	v_mfma_f32_16x16x32_bf16 v[86:89], v[130:133], v[86:89], v[0:3]
	v_mfma_f32_16x16x32_bf16 v[52:55], v[126:129], v[48:51], v[52:55]
	s_waitcnt lgkmcnt(0)
	v_mfma_f32_16x16x32_bf16 v[48:51], v[134:137], v[48:51], v[86:89]
	s_cbranch_scc1 .LBB0_414
	s_nop 3
	v_pk_add_f32 v[86:87], v[84:85], s[84:85] op_sel_hi:[1,0]
	v_pk_add_f32 v[88:89], v[82:83], s[84:85] op_sel_hi:[1,0]
	v_cndmask_b32_e64 v85, v85, v87, s[20:21]
	v_cndmask_b32_e64 v84, v84, v86, s[20:21]
	v_cndmask_b32_e64 v83, v83, v89, s[20:21]
	v_cndmask_b32_e64 v82, v82, v88, s[20:21]
	v_pk_add_f32 v[86:87], v[80:81], s[84:85] op_sel_hi:[1,0]
	v_pk_add_f32 v[88:89], v[78:79], s[84:85] op_sel_hi:[1,0]
	v_cndmask_b32_e64 v81, v81, v87, s[18:19]
	v_cndmask_b32_e64 v80, v80, v86, s[18:19]
	v_cndmask_b32_e64 v79, v79, v89, s[18:19]
	v_cndmask_b32_e64 v78, v78, v88, s[18:19]
	v_pk_add_f32 v[86:87], v[76:77], s[84:85] op_sel_hi:[1,0]
	v_pk_add_f32 v[88:89], v[74:75], s[84:85] op_sel_hi:[1,0]
	v_cndmask_b32_e64 v77, v77, v87, s[16:17]
	v_cndmask_b32_e64 v76, v76, v86, s[16:17]
	v_cndmask_b32_e64 v75, v75, v89, s[16:17]
	v_cndmask_b32_e64 v74, v74, v88, s[16:17]
	v_pk_add_f32 v[86:87], v[72:73], s[84:85] op_sel_hi:[1,0]
	v_pk_add_f32 v[88:89], v[70:71], s[84:85] op_sel_hi:[1,0]
	v_cndmask_b32_e64 v73, v73, v87, s[14:15]
	v_cndmask_b32_e64 v72, v72, v86, s[14:15]
	v_cndmask_b32_e64 v71, v71, v89, s[14:15]
	v_cndmask_b32_e64 v70, v70, v88, s[14:15]
	v_pk_add_f32 v[86:87], v[68:69], s[84:85] op_sel_hi:[1,0]
	v_pk_add_f32 v[88:89], v[66:67], s[84:85] op_sel_hi:[1,0]
	v_cndmask_b32_e64 v69, v69, v87, s[12:13]
	v_cndmask_b32_e64 v68, v68, v86, s[12:13]
	v_cndmask_b32_e64 v67, v67, v89, s[12:13]
	v_cndmask_b32_e64 v66, v66, v88, s[12:13]
	v_pk_add_f32 v[86:87], v[62:63], s[84:85] op_sel_hi:[1,0]
	v_pk_add_f32 v[88:89], v[60:61], s[84:85] op_sel_hi:[1,0]
	v_cndmask_b32_e64 v63, v63, v87, s[10:11]
	v_cndmask_b32_e64 v62, v62, v86, s[10:11]
	v_cndmask_b32_e64 v61, v61, v89, s[10:11]
	v_cndmask_b32_e64 v60, v60, v88, s[10:11]
	v_pk_add_f32 v[86:87], v[58:59], s[84:85] op_sel_hi:[1,0]
	v_pk_add_f32 v[88:89], v[56:57], s[84:85] op_sel_hi:[1,0]
	v_cndmask_b32_e64 v59, v59, v87, s[8:9]
	v_cndmask_b32_e64 v58, v58, v86, s[8:9]
	v_cndmask_b32_e64 v57, v57, v89, s[8:9]
	v_cndmask_b32_e64 v56, v56, v88, s[8:9]
	v_pk_add_f32 v[86:87], v[54:55], s[84:85] op_sel_hi:[1,0]
	v_pk_add_f32 v[88:89], v[52:53], s[84:85] op_sel_hi:[1,0]
	v_cndmask_b32_e64 v55, v55, v87, s[6:7]
	v_cndmask_b32_e64 v54, v54, v86, s[6:7]
	v_cndmask_b32_e64 v53, v53, v89, s[6:7]
	v_cndmask_b32_e64 v52, v52, v88, s[6:7]
.LBB0_414:
	v_add3_u32 v64, s101, v173, v171
	ds_read_b64_tr_b16 v[90:91], v64 offset:36864
	s_nop 1
	ds_read_b64_tr_b16 v[86:87], v64 offset:36896
	ds_read_b64_tr_b16 v[100:101], v64 offset:36928
	ds_read_b64_tr_b16 v[108:109], v64 offset:36960
	ds_read_b64_tr_b16 v[92:93], v64 offset:39168
	ds_read_b64_tr_b16 v[88:89], v64 offset:39200
	ds_read_b64_tr_b16 v[102:103], v64 offset:39232
	ds_read_b64_tr_b16 v[110:111], v64 offset:39264
	ds_read_b64_tr_b16 v[104:105], v64 offset:41472
	ds_read_b64_tr_b16 v[112:113], v64 offset:41504
	ds_read_b64_tr_b16 v[118:119], v64 offset:41536
	ds_read_b64_tr_b16 v[126:127], v64 offset:41568
	ds_read_b64_tr_b16 v[106:107], v64 offset:43776
	ds_read_b64_tr_b16 v[114:115], v64 offset:43808
	ds_read_b64_tr_b16 v[120:121], v64 offset:43840
	ds_read_b64_tr_b16 v[128:129], v64 offset:43872
	ds_read_b64_tr_b16 v[122:123], v64 offset:46080
	ds_read_b64_tr_b16 v[130:131], v64 offset:46112
	ds_read_b64_tr_b16 v[138:139], v64 offset:46144
	ds_read_b64_tr_b16 v[146:147], v64 offset:46176
	ds_read_b64_tr_b16 v[124:125], v64 offset:48384
	ds_read_b64_tr_b16 v[132:133], v64 offset:48416
	ds_read_b64_tr_b16 v[140:141], v64 offset:48448
	ds_read_b64_tr_b16 v[148:149], v64 offset:48480
	ds_read_b64_tr_b16 v[142:143], v64 offset:50688
	ds_read_b64_tr_b16 v[152:153], v64 offset:50720
	ds_read_b64_tr_b16 v[156:157], v64 offset:50752
	ds_read_b64_tr_b16 v[134:135], v64 offset:50784
	ds_read_b64_tr_b16 v[144:145], v64 offset:52992
	ds_read_b64_tr_b16 v[154:155], v64 offset:53024
	ds_read_b64_tr_b16 v[158:159], v64 offset:53056
	ds_read_b64_tr_b16 v[136:137], v64 offset:53088
	ds_read_b64_tr_b16 v[150:151], v64 offset:55296
	ds_read_b64_tr_b16 v[116:117], v64 offset:55328
	ds_read_b64_tr_b16 v[98:99], v64 offset:55360
	ds_read_b64_tr_b16 v[94:95], v64 offset:55392
	v_max3_f32 v64, v82, s84, v83
	v_max3_f32 v64, v64, v84, v85
	v_max3_f32 v64, v64, v78, v79
	v_max3_f32 v64, v64, v80, v81
	v_max3_f32 v64, v64, v74, v75
	v_max3_f32 v64, v64, v76, v77
	v_max3_f32 v64, v64, v70, v71
	v_max3_f32 v64, v64, v72, v73
	v_max3_f32 v64, v64, v66, v67
	v_max3_f32 v64, v64, v68, v69
	v_max3_f32 v64, v64, v60, v61
	v_max3_f32 v64, v64, v62, v63
	v_max3_f32 v64, v64, v56, v57
	v_max3_f32 v64, v64, v58, v59
	v_max3_f32 v64, v64, v52, v53
	v_max3_f32 v64, v64, v54, v55
	v_max3_f32 v64, v64, v48, v49
	v_max3_f32 v64, v64, v50, v51
	v_mov_b32_e32 v96, v64
	s_nop 1
	v_permlane16_swap_b32_e32 v64, v96
	v_max_f32_e32 v64, v64, v96
	v_mov_b32_e32 v96, v64
	s_nop 1
	v_permlane32_swap_b32_e32 v64, v96
	v_max_f32_e32 v170, v64, v96
	v_pk_add_f32 v[82:83], v[82:83], v[170:171] op_sel_hi:[1,0] neg_lo:[0,1] neg_hi:[0,1]
	v_pk_add_f32 v[84:85], v[84:85], v[170:171] op_sel_hi:[1,0] neg_lo:[0,1] neg_hi:[0,1]
	v_exp_f32_e32 v82, v82
	v_exp_f32_e32 v83, v83
	v_exp_f32_e32 v84, v84
	v_exp_f32_e32 v85, v85
	v_pk_add_f32 v[78:79], v[78:79], v[170:171] op_sel_hi:[1,0] neg_lo:[0,1] neg_hi:[0,1]
	v_pk_add_f32 v[80:81], v[80:81], v[170:171] op_sel_hi:[1,0] neg_lo:[0,1] neg_hi:[0,1]
	v_exp_f32_e32 v78, v78
	v_exp_f32_e32 v79, v79
	v_exp_f32_e32 v80, v80
	v_exp_f32_e32 v81, v81
	v_pk_add_f32 v[74:75], v[74:75], v[170:171] op_sel_hi:[1,0] neg_lo:[0,1] neg_hi:[0,1]
	v_pk_add_f32 v[76:77], v[76:77], v[170:171] op_sel_hi:[1,0] neg_lo:[0,1] neg_hi:[0,1]
	v_exp_f32_e32 v192, v74
	v_exp_f32_e32 v193, v75
	v_pk_add_f32 v[96:97], v[84:85], v[82:83]
	v_exp_f32_e32 v194, v76
	v_exp_f32_e32 v195, v77
	v_pk_add_f32 v[70:71], v[70:71], v[170:171] op_sel_hi:[1,0] neg_lo:[0,1] neg_hi:[0,1]
	v_pk_add_f32 v[74:75], v[78:79], v[96:97]
	v_pk_add_f32 v[72:73], v[72:73], v[170:171] op_sel_hi:[1,0] neg_lo:[0,1] neg_hi:[0,1]
	v_exp_f32_e32 v96, v70
	v_exp_f32_e32 v97, v71
	v_pk_add_f32 v[74:75], v[80:81], v[74:75]
	v_exp_f32_e32 v196, v72
	v_exp_f32_e32 v197, v73
	v_pk_add_f32 v[66:67], v[66:67], v[170:171] op_sel_hi:[1,0] neg_lo:[0,1] neg_hi:[0,1]
	v_pk_add_f32 v[74:75], v[192:193], v[74:75]
	v_pk_add_f32 v[68:69], v[68:69], v[170:171] op_sel_hi:[1,0] neg_lo:[0,1] neg_hi:[0,1]
	v_exp_f32_e32 v198, v66
	v_exp_f32_e32 v199, v67
	v_pk_add_f32 v[74:75], v[194:195], v[74:75]
	v_exp_f32_e32 v200, v68
	v_exp_f32_e32 v201, v69
	v_pk_add_f32 v[66:67], v[96:97], v[74:75]
	v_cvt_pk_bf16_f32 v68, v78, v79
	v_pk_add_f32 v[66:67], v[196:197], v[66:67]
	v_cvt_pk_bf16_f32 v69, v80, v81
	v_pk_add_f32 v[66:67], v[198:199], v[66:67]
	v_pk_add_f32 v[74:75], v[60:61], v[170:171] op_sel_hi:[1,0] neg_lo:[0,1] neg_hi:[0,1]
	v_pk_add_f32 v[202:203], v[200:201], v[66:67]
	v_cvt_pk_bf16_f32 v66, v82, v83
	v_cvt_pk_bf16_f32 v67, v84, v85
	v_pk_add_f32 v[76:77], v[62:63], v[170:171] op_sel_hi:[1,0] neg_lo:[0,1] neg_hi:[0,1]
	v_exp_f32_e32 v78, v74
	s_waitcnt lgkmcnt(14)
	v_mfma_f32_16x16x32_bf16 v[70:73], v[90:93], v[66:69], 0
	v_exp_f32_e32 v79, v75
	v_exp_f32_e32 v80, v76
	v_exp_f32_e32 v81, v77
	v_mfma_f32_16x16x32_bf16 v[60:63], v[86:89], v[66:69], 0
	v_add_f32_e64 v84, v56, -v170
	v_add_f32_e64 v85, v57, -v170
	v_pk_add_f32 v[86:87], v[58:59], v[170:171] op_sel_hi:[1,0] neg_lo:[0,1] neg_hi:[0,1]
	v_exp_f32_e32 v84, v84
	v_mfma_f32_16x16x32_bf16 v[74:77], v[100:103], v[66:69], 0
	v_exp_f32_e32 v85, v85
	v_exp_f32_e32 v86, v86
	v_exp_f32_e32 v87, v87
	v_mfma_f32_16x16x32_bf16 v[56:59], v[108:111], v[66:69], 0
	v_cvt_pk_bf16_f32 v66, v192, v193
	v_cvt_pk_bf16_f32 v67, v194, v195
	v_cvt_pk_bf16_f32 v68, v96, v97
	v_cvt_pk_bf16_f32 v69, v196, v197
	v_pk_add_f32 v[88:89], v[52:53], v[170:171] op_sel_hi:[1,0] neg_lo:[0,1] neg_hi:[0,1]
	v_pk_add_f32 v[82:83], v[78:79], v[202:203]
	v_mfma_f32_16x16x32_bf16 v[70:73], v[104:107], v[66:69], v[70:73]
	v_add_f32_e64 v90, v54, -v170
	v_add_f32_e64 v91, v55, -v170
	v_pk_add_f32 v[82:83], v[80:81], v[82:83]
	v_pk_add_f32 v[48:49], v[48:49], v[170:171] op_sel_hi:[1,0] neg_lo:[0,1] neg_hi:[0,1]
	v_mfma_f32_16x16x32_bf16 v[60:63], v[112:115], v[66:69], v[60:63]
	v_add_f32_e64 v82, v84, v82
	v_add_f32_e64 v83, v85, v83
	s_waitcnt lgkmcnt(1)
	v_mov_b32_e32 v100, v98
	v_pk_add_f32 v[82:83], v[86:87], v[82:83]
	v_mfma_f32_16x16x32_bf16 v[74:77], v[118:121], v[66:69], v[74:77]
	v_mov_b32_e32 v118, v116
	v_mov_b32_e32 v119, v117
	v_mov_b32_e32 v101, v99
	v_mfma_f32_16x16x32_bf16 v[52:55], v[126:129], v[66:69], v[56:59]
	s_waitcnt lgkmcnt(0)
	v_mov_b32_e32 v96, v94
	v_mov_b32_e32 v97, v95
	v_mov_b32_e32 v64, v65
	v_cvt_pk_bf16_f32 v58, v78, v79
	v_exp_f32_e32 v78, v88
	v_exp_f32_e32 v79, v89
	v_cvt_pk_bf16_f32 v56, v198, v199
	v_cvt_pk_bf16_f32 v57, v200, v201
	v_cvt_pk_bf16_f32 v59, v80, v81
	v_exp_f32_e32 v80, v90
	v_exp_f32_e32 v81, v91
	v_mfma_f32_16x16x32_bf16 v[66:69], v[122:125], v[56:59], v[70:73]
	v_add_f32_e64 v82, v78, v82
	v_add_f32_e64 v83, v79, v83
	s_cmp_eq_u32 s30, 1
	s_mov_b32 s23, 0xe800000
	v_mfma_f32_16x16x32_bf16 v[60:63], v[130:133], v[56:59], v[60:63]
	s_cselect_b32 s23, s23, 0x2e800000
	s_cmp_lg_u32 s30, 0
	s_cselect_b32 s23, s23, 0x12800000
	v_mfma_f32_16x16x32_bf16 v[70:73], v[138:141], v[56:59], v[74:77]
	s_add_u32 s36, s42, s23
	s_addc_u32 s37, s43, 0
	s_lshl_b32 s66, s22, 6
	v_pk_add_f32 v[74:75], v[50:51], v[170:171] op_sel_hi:[1,0] neg_lo:[0,1] neg_hi:[0,1]
	v_exp_f32_e32 v76, v48
	v_exp_f32_e32 v77, v49
	v_exp_f32_e32 v74, v74
	v_exp_f32_e32 v75, v75
	v_mfma_f32_16x16x32_bf16 v[48:51], v[146:149], v[56:59], v[52:55]
	s_nop 2
	v_cvt_pk_bf16_f32 v52, v84, v85
	v_cvt_pk_bf16_f32 v53, v86, v87
	v_cvt_pk_bf16_f32 v54, v78, v79
	v_cvt_pk_bf16_f32 v55, v80, v81
	v_pk_add_f32 v[78:79], v[80:81], v[82:83]
	s_nop 0
	v_mfma_f32_16x16x32_bf16 v[56:59], v[142:145], v[52:55], v[66:69]
	v_mfma_f32_16x16x32_bf16 v[66:69], v[152:155], v[52:55], v[60:63]
	v_mov_b32_e32 v152, v150
	v_mov_b32_e32 v153, v151
	s_nop 0
	v_pk_add_f32 v[60:61], v[76:77], v[78:79]
	v_mfma_f32_16x16x32_bf16 v[70:73], v[156:159], v[52:55], v[70:73]
	v_add_f32_e64 v60, v74, v60
	v_add_f32_e64 v61, v75, v61
	v_cvt_pk_bf16_f32 v62, v76, v77
	v_pk_add_f32 v[60:61], v[60:61], v[60:61] op_sel:[0,1] op_sel_hi:[1,0]
	v_mfma_f32_16x16x32_bf16 v[48:51], v[134:137], v[52:55], v[48:51]
	v_mov_b32_e32 v61, v60
	s_nop 1
	v_permlane16_swap_b32_e32 v60, v61
	v_cvt_pk_bf16_f32 v63, v74, v75
	v_add_f32_e32 v74, v60, v61
	s_nop 0
	v_mfma_f32_16x16x32_bf16 v[52:55], v[150:153], v[62:65], v[56:59]
	v_mfma_f32_16x16x32_bf16 v[56:59], v[116:119], v[62:65], v[66:69]
	v_mfma_f32_16x16x32_bf16 v[66:69], v[98:101], v[62:65], v[70:73]
	s_nop 2
	v_mov_b32_e32 v70, v74
	s_nop 1
	v_permlane32_swap_b32_e32 v74, v70
	v_mfma_f32_16x16x32_bf16 v[60:63], v[94:97], v[62:65], v[48:51]
	s_nop 2
	v_add_f32_e32 v48, v74, v70
	v_rcp_f32_e32 v49, v48
	s_nop 0
	v_mul_f32_e32 v206, 0x42800000, v49
	v_add3_u32 v226, s100, v177, v176
	s_waitcnt vmcnt(9)
	ds_write_b128 v226, v[16:19]
	v_pk_mul_f32 v[208:209], v[52:53], v[206:207] op_sel_hi:[1,0]
	v_pk_mul_f32 v[210:211], v[54:55], v[206:207] op_sel_hi:[1,0]
	v_pk_mul_f32 v[212:213], v[56:57], v[206:207] op_sel_hi:[1,0]
	v_pk_mul_f32 v[216:217], v[58:59], v[206:207] op_sel_hi:[1,0]
	s_waitcnt vmcnt(8)
	ds_write_b128 v226, v[20:23] offset:36864
	v_pk_mul_f32 v[218:219], v[66:67], v[206:207] op_sel_hi:[1,0]
	v_pk_mul_f32 v[220:221], v[68:69], v[206:207] op_sel_hi:[1,0]
	v_pk_mul_f32 v[222:223], v[60:61], v[206:207] op_sel_hi:[1,0]
	v_pk_mul_f32 v[224:225], v[62:63], v[206:207] op_sel_hi:[1,0]
	v_add3_u32 v226, s100, v178, v176
	s_waitcnt vmcnt(7)
	ds_write_b128 v226, v[24:27]
	v_med3_f32 v208, v208, s55, v228
	v_med3_f32 v209, v209, s55, v228
	v_med3_f32 v210, v210, s55, v228
	v_med3_f32 v211, v211, s55, v228
	s_waitcnt vmcnt(6)
	ds_write_b128 v226, v[28:31] offset:36864
	v_med3_f32 v212, v212, s55, v228
	v_med3_f32 v213, v213, s55, v228
	v_med3_f32 v216, v216, s55, v228
	v_med3_f32 v217, v217, s55, v228
	v_add3_u32 v226, s100, v179, v176
	s_waitcnt vmcnt(5)
	ds_write_b128 v226, v[32:35]
	v_med3_f32 v218, v218, s55, v228
	v_med3_f32 v219, v219, s55, v228
	v_med3_f32 v220, v220, s55, v228
	v_med3_f32 v221, v221, s55, v228
	s_waitcnt vmcnt(4)
	ds_write_b128 v226, v[36:39] offset:36864
	v_med3_f32 v222, v222, s55, v228
	v_med3_f32 v223, v223, s55, v228
	v_med3_f32 v224, v224, s55, v228
	v_med3_f32 v225, v225, s55, v228
	v_add3_u32 v226, s100, v180, v176
	s_waitcnt vmcnt(3)
	ds_write_b128 v226, v[40:43]
	v_cvt_pk_fp8_f32 v50, v208, v209
	v_cvt_pk_fp8_f32 v50, v210, v211 op_sel:[0,0,1]
	v_cvt_pk_fp8_f32 v51, v212, v213
	v_cvt_pk_fp8_f32 v51, v216, v217 op_sel:[0,0,1]
	s_waitcnt vmcnt(2)
	ds_write_b128 v226, v[44:47] offset:36864
	v_cvt_pk_fp8_f32 v52, v218, v219
	v_cvt_pk_fp8_f32 v52, v220, v221 op_sel:[0,0,1]
	v_cvt_pk_fp8_f32 v53, v222, v223
	v_cvt_pk_fp8_f32 v53, v224, v225 op_sel:[0,0,1]
	v_lshlrev_b64 v[54:55], 10, v[166:167]
	v_lshl_add_u64 v[54:55], s[36:37], 0, v[54:55]
	v_lshl_add_u64 v[54:55], v[54:55], 0, s[66:67]
	v_lshl_add_u64 v[54:55], v[54:55], 0, v[160:161]
	global_store_dwordx4 v[54:55], v[50:53], off sc1
	s_and_saveexec_b64 s[36:37], vcc
	s_cbranch_execz .LBB0_416
	v_log_f32_e32 v48, v48
	s_ashr_i32 s31, s30, 31
	s_lshl_b64 s[30:31], s[30:31], 22
	v_readlane_b32 s23, v254, 30
	s_add_u32 s30, s23, s30
	v_readlane_b32 s23, v254, 31
	v_add_f32_e32 v48, v170, v48
	s_addc_u32 s31, s23, s31
	v_mul_f32_e32 v50, 0x3f317218, v48
	v_lshlrev_b64 v[48:49], 6, v[166:167]
	v_lshl_add_u64 v[48:49], s[30:31], 0, v[48:49]
	s_mov_b32 s23, s67
	v_lshl_add_u64 v[48:49], s[22:23], 2, v[48:49]
	global_store_dword v[48:49], v50, off
